# v83 + CB0 token loop software-pipelined: next token's 20 row loads issued before the current token is combined (second register set + copy)
# baseline (speedup 1.0000x reference)
.LBB0_970:
	s_or_b64 exec, exec, s[0:1]
	s_waitcnt lgkmcnt(0)
	s_barrier
	s_getreg_b32 s0, hwreg(HW_REG_HW_ID, 0, 6)
	s_lshl_b32 s0, s0, 2
	s_add_i32 s0, s0, 0x27000
	v_mov_b32_e32 v0, s0
	ds_read_b32 v0, v0
	v_mov_b32_e32 v1, 0
	v_mov_b32_e32 v4, 0
	s_waitcnt lgkmcnt(0)
	v_readfirstlane_b32 s0, v0
	v_mbcnt_lo_u32_b32 v0, -1, v1
	v_mbcnt_hi_u32_b32 v0, -1, v0
	v_lshl_or_b32 v2, s0, 6, v0
	s_getreg_b32 s0, hwreg(HW_REG_HW_ID, 0, 6)
	s_lshl_b32 s0, s0, 2
	s_add_i32 s0, s0, 0x27000
	v_mov_b32_e32 v0, s0
	ds_read_b32 v0, v0
	v_mov_b32_e32 v1, 0
	s_waitcnt lgkmcnt(0)
	v_readfirstlane_b32 s0, v0
	v_mbcnt_lo_u32_b32 v0, -1, v1
	v_mbcnt_hi_u32_b32 v0, -1, v0
	v_lshl_or_b32 v3, s0, 6, v0
	s_getreg_b32 s0, hwreg(HW_REG_HW_ID, 0, 6)
	s_lshl_b32 s0, s0, 2
	s_add_i32 s0, s0, 0x27000
	v_mov_b32_e32 v0, s0
	ds_read_b32 v0, v0
	v_mov_b32_e32 v1, 0
	s_waitcnt lgkmcnt(0)
	v_readfirstlane_b32 s0, v0
	v_mbcnt_lo_u32_b32 v0, -1, v4
	v_mbcnt_hi_u32_b32 v0, -1, v0
	v_lshl_or_b32 v0, s0, 6, v0
	s_movk_i32 s0, 0x100
	s_nop 0
	v_cmp_gt_i32_e32 vcc, s0, v0
	v_lshl_add_u32 v4, v0, 2, 0
	v_ashrrev_i32_e32 v0, 6, v3
	v_readlane_b32 s0, v253, 30
	s_waitcnt lgkmcnt(0)
	s_barrier
	v_add_u32_e32 v80, s0, v0
	s_movk_i32 s0, 0x4000
	v_cmp_gt_i32_e32 vcc, s0, v80
	s_and_saveexec_b64 s[2:3], vcc
	s_cbranch_execz .LBB0_1014
	v_readlane_b32 s4, v253, 4
	v_and_b32_e32 v1, 63, v2
	v_readlane_b32 s5, v253, 5
	v_lshlrev_b32_e32 v2, 5, v1
	v_mov_b32_e32 v3, 0
	v_readlane_b32 s18, v253, 18
	v_readlane_b32 s19, v253, 19
	v_readlane_b32 s4, v254, 3
	v_lshl_add_u64 v[84:85], s[64:65], 0, v[2:3]
	v_lshl_add_u64 v[82:83], s[18:19], 0, v[2:3]
	v_lshlrev_b32_e32 v2, 4, v1
	v_readlane_b32 s5, v254, 4
	v_lshlrev_b32_e32 v0, 3, v0
	v_ashrrev_i32_e32 v81, 31, v80
	v_lshl_add_u64 v[86:87], s[4:5], 0, v[2:3]
	s_lshl_b32 s4, s72, 6
	v_cmp_gt_u32_e64 s[0:1], 8, v1
	v_add3_u32 v88, s4, v0, v1
	v_readlane_b32 s4, v253, 2
	v_lshlrev_b64 v[0:1], 11, v[80:81]
	v_readlane_b32 s9, v253, 9
	v_readlane_b32 s5, v253, 3
	v_or_b32_e32 v0, v0, v2
	v_readlane_b32 s6, v253, 6
	v_readlane_b32 s7, v253, 7
	v_readlane_b32 s8, v253, 8
	s_lshl_b32 s9, s4, 6
	v_lshl_add_u64 v[0:1], s[70:71], 0, v[0:1]
	s_mov_b64 s[4:5], 0xd60d500
	s_ashr_i32 s75, s74, 31
	v_lshl_add_u64 v[90:91], v[0:1], 0, s[4:5]
	s_lshl_b64 s[4:5], s[74:75], 11
	s_mov_b64 s[6:7], 0
	s_mov_b32 s8, 0x3fb504f3
	v_mov_b32_e32 v81, 0x3727c5ac
	v_readlane_b32 s10, v253, 10
	v_readlane_b32 s11, v253, 11
	v_readlane_b32 s12, v253, 12
	v_readlane_b32 s13, v253, 13
	v_readlane_b32 s14, v253, 14
	v_readlane_b32 s15, v253, 15
	v_readlane_b32 s16, v253, 16
	v_readlane_b32 s17, v253, 17
	v_min_u32_e32 v240, 0x1ffff, v88
	v_mov_b32_e32 v241, 0
	v_readlane_b32 s98, v253, 55
	v_readlane_b32 s99, v253, 56
	v_lshlrev_b64 v[240:241], 2, v[240:241]
	s_nop 1
	v_lshl_add_u64 v[242:243], s[98:99], 0, v[240:241]
	global_load_dword v244, v[242:243], off
	v_readlane_b32 s98, v253, 59
	v_readlane_b32 s99, v253, 60
	s_nop 1
	v_lshl_add_u64 v[242:243], s[98:99], 0, v[240:241]
	global_load_dword v245, v[242:243], off
	v_readlane_b32 s98, v253, 57
	v_readlane_b32 s99, v253, 58
	s_nop 1
	v_lshl_add_u64 v[242:243], s[98:99], 0, v[240:241]
	global_load_dword v246, v[242:243], off
	global_load_dwordx4 v[200:203], v[82:83], off
	global_load_dwordx4 v[204:207], v[82:83], off offset:16
	global_load_dwordx4 v[208:211], v[84:85], off
	global_load_dwordx4 v[212:215], v[84:85], off offset:16
	global_load_dwordx4 v[216:219], v[82:83], off offset:2048
	global_load_dwordx4 v[220:223], v[82:83], off offset:2064
	global_load_dwordx4 v[224:227], v[84:85], off offset:2048
	global_load_dwordx4 v[228:231], v[84:85], off offset:2064
	s_waitcnt vmcnt(0)
	v_lshl_add_u32 v249, v244, 2, 0
	v_add_u32_e32 v249, 0x1ec10, v249
	ds_read_b32 v249, v249
	s_waitcnt lgkmcnt(0)
	v_add_u32_e32 v248, v245, v249
	v_cndmask_b32_e64 v248, 0, v248, s[0:1]
	v_cndmask_b32_e64 v247, 0, v246, s[0:1]
	v_mov_b32_e32 v250, v80
	v_mov_b32_e32 v232, v90
	v_mov_b32_e32 v233, v91
	global_load_dwordx4 v[172:175], v[232:233], off
	global_load_dwordx4 v[132:135], v[232:233], off offset:1024
	v_add_u32_e32 v234, 0x20000, v250
	v_ashrrev_i32_e32 v235, 31, v234
	v_lshlrev_b64 v[234:235], 11, v[234:235]
	v_lshl_add_u64 v[234:235], v[86:87], 0, v[234:235]
	global_load_dwordx4 v[168:171], v[234:235], off
	global_load_dwordx4 v[128:131], v[234:235], off offset:1024
	v_readlane_b32 s98, v248, 0
	s_ashr_i32 s99, s98, 31
	s_lshl_b64 s[98:99], s[98:99], 11
	v_lshl_add_u64 v[234:235], v[86:87], 0, s[98:99]
	global_load_dwordx4 v[176:179], v[234:235], off
	global_load_dwordx4 v[140:143], v[234:235], off offset:1024
	v_readlane_b32 s98, v248, 1
	s_ashr_i32 s99, s98, 31
	s_lshl_b64 s[98:99], s[98:99], 11
	v_lshl_add_u64 v[234:235], v[86:87], 0, s[98:99]
	global_load_dwordx4 v[180:183], v[234:235], off
	global_load_dwordx4 v[148:151], v[234:235], off offset:1024
	v_readlane_b32 s98, v248, 2
	s_ashr_i32 s99, s98, 31
	s_lshl_b64 s[98:99], s[98:99], 11
	v_lshl_add_u64 v[234:235], v[86:87], 0, s[98:99]
	global_load_dwordx4 v[188:191], v[234:235], off
	global_load_dwordx4 v[156:159], v[234:235], off offset:1024
	v_readlane_b32 s98, v248, 3
	s_ashr_i32 s99, s98, 31
	s_lshl_b64 s[98:99], s[98:99], 11
	v_lshl_add_u64 v[234:235], v[86:87], 0, s[98:99]
	global_load_dwordx4 v[192:195], v[234:235], off
	global_load_dwordx4 v[160:163], v[234:235], off offset:1024
	v_readlane_b32 s98, v248, 4
	s_ashr_i32 s99, s98, 31
	s_lshl_b64 s[98:99], s[98:99], 11
	v_lshl_add_u64 v[234:235], v[86:87], 0, s[98:99]
	global_load_dwordx4 v[196:199], v[234:235], off
	global_load_dwordx4 v[164:167], v[234:235], off offset:1024
	v_readlane_b32 s98, v248, 5
	s_ashr_i32 s99, s98, 31
	s_lshl_b64 s[98:99], s[98:99], 11
	v_lshl_add_u64 v[234:235], v[86:87], 0, s[98:99]
	global_load_dwordx4 v[136:139], v[234:235], off
	global_load_dwordx4 v[120:123], v[234:235], off offset:1024
	v_readlane_b32 s98, v248, 6
	s_ashr_i32 s99, s98, 31
	s_lshl_b64 s[98:99], s[98:99], 11
	v_lshl_add_u64 v[234:235], v[86:87], 0, s[98:99]
	global_load_dwordx4 v[152:155], v[234:235], off
	global_load_dwordx4 v[124:127], v[234:235], off offset:1024
	v_readlane_b32 s98, v248, 7
	s_ashr_i32 s99, s98, 31
	s_lshl_b64 s[98:99], s[98:99], 11
	v_lshl_add_u64 v[234:235], v[86:87], 0, s[98:99]
	global_load_dwordx4 v[184:187], v[234:235], off
	global_load_dwordx4 v[144:147], v[234:235], off offset:1024
	v_add_u32_e32 v88, s9, v88
	v_min_u32_e32 v240, 0x1ffff, v88
	v_mov_b32_e32 v241, 0
	v_readlane_b32 s98, v253, 55
	v_readlane_b32 s99, v253, 56
	v_lshlrev_b64 v[240:241], 2, v[240:241]
	s_nop 1
	v_lshl_add_u64 v[242:243], s[98:99], 0, v[240:241]
	global_load_dword v244, v[242:243], off
	v_readlane_b32 s98, v253, 59
	v_readlane_b32 s99, v253, 60
	s_nop 1
	v_lshl_add_u64 v[242:243], s[98:99], 0, v[240:241]
	global_load_dword v245, v[242:243], off
	v_readlane_b32 s98, v253, 57
	v_readlane_b32 s99, v253, 58
	s_nop 1
	v_lshl_add_u64 v[242:243], s[98:99], 0, v[240:241]
	global_load_dword v246, v[242:243], off
	s_waitcnt vmcnt(0)
	s_branch .Lopt21_cb0_top2

.Lopt21_cb0_top2:
	v_readlane_b32 s24, v247, 0
	v_readlane_b32 s10, v247, 1
	v_readlane_b32 s12, v247, 2
	v_readlane_b32 s14, v247, 3
	v_readlane_b32 s16, v247, 4
	v_readlane_b32 s18, v247, 5
	v_readlane_b32 s20, v247, 6
	v_readlane_b32 s22, v247, 7
	v_mov_b32_e32 v0, v120
	v_mov_b32_e32 v1, v121
	v_mov_b32_e32 v2, v122
	v_mov_b32_e32 v3, v123
	v_mov_b32_e32 v4, v124
	v_mov_b32_e32 v5, v125
	v_mov_b32_e32 v6, v126
	v_mov_b32_e32 v7, v127
	v_mov_b32_e32 v8, v128
	v_mov_b32_e32 v9, v129
	v_mov_b32_e32 v10, v130
	v_mov_b32_e32 v11, v131
	v_mov_b32_e32 v12, v132
	v_mov_b32_e32 v13, v133
	v_mov_b32_e32 v14, v134
	v_mov_b32_e32 v15, v135
	v_mov_b32_e32 v16, v136
	v_mov_b32_e32 v17, v137
	v_mov_b32_e32 v18, v138
	v_mov_b32_e32 v19, v139
	v_mov_b32_e32 v20, v140
	v_mov_b32_e32 v21, v141
	v_mov_b32_e32 v22, v142
	v_mov_b32_e32 v23, v143
	v_mov_b32_e32 v24, v144
	v_mov_b32_e32 v25, v145
	v_mov_b32_e32 v26, v146
	v_mov_b32_e32 v27, v147
	v_mov_b32_e32 v28, v148
	v_mov_b32_e32 v29, v149
	v_mov_b32_e32 v30, v150
	v_mov_b32_e32 v31, v151
	v_mov_b32_e32 v32, v152
	v_mov_b32_e32 v33, v153
	v_mov_b32_e32 v34, v154
	v_mov_b32_e32 v35, v155
	v_mov_b32_e32 v36, v156
	v_mov_b32_e32 v37, v157
	v_mov_b32_e32 v38, v158
	v_mov_b32_e32 v39, v159
	v_mov_b32_e32 v40, v160
	v_mov_b32_e32 v41, v161
	v_mov_b32_e32 v42, v162
	v_mov_b32_e32 v43, v163
	v_mov_b32_e32 v44, v164
	v_mov_b32_e32 v45, v165
	v_mov_b32_e32 v46, v166
	v_mov_b32_e32 v47, v167
	v_mov_b32_e32 v48, v168
	v_mov_b32_e32 v49, v169
	v_mov_b32_e32 v50, v170
	v_mov_b32_e32 v51, v171
	v_mov_b32_e32 v52, v172
	v_mov_b32_e32 v53, v173
	v_mov_b32_e32 v54, v174
	v_mov_b32_e32 v55, v175
	v_mov_b32_e32 v56, v176
	v_mov_b32_e32 v57, v177
	v_mov_b32_e32 v58, v178
	v_mov_b32_e32 v59, v179
	v_mov_b32_e32 v60, v180
	v_mov_b32_e32 v61, v181
	v_mov_b32_e32 v62, v182
	v_mov_b32_e32 v63, v183
	v_mov_b32_e32 v64, v184
	v_mov_b32_e32 v65, v185
	v_mov_b32_e32 v66, v186
	v_mov_b32_e32 v67, v187
	v_mov_b32_e32 v68, v188
	v_mov_b32_e32 v69, v189
	v_mov_b32_e32 v70, v190
	v_mov_b32_e32 v71, v191
	v_mov_b32_e32 v72, v192
	v_mov_b32_e32 v73, v193
	v_mov_b32_e32 v74, v194
	v_mov_b32_e32 v75, v195
	v_mov_b32_e32 v76, v196
	v_mov_b32_e32 v77, v197
	v_mov_b32_e32 v78, v198
	v_mov_b32_e32 v79, v199
	v_lshl_add_u32 v249, v244, 2, 0
	v_add_u32_e32 v249, 0x1ec10, v249
	ds_read_b32 v249, v249
	s_waitcnt lgkmcnt(0)
	v_add_u32_e32 v248, v245, v249
	v_cndmask_b32_e64 v248, 0, v248, s[0:1]
	v_cndmask_b32_e64 v247, 0, v246, s[0:1]
	v_add_u32_e32 v250, s74, v80
	v_cmp_gt_i32_e32 vcc, 0x4000, v250
	v_lshl_add_u64 v[232:233], v[90:91], 0, s[4:5]
	s_nop 1
	v_cndmask_b32_e32 v232, v90, v232, vcc
	v_cndmask_b32_e32 v233, v91, v233, vcc
	v_cndmask_b32_e32 v250, v80, v250, vcc
	v_add_u32_e32 v80, s74, v80
	global_load_dwordx4 v[172:175], v[232:233], off
	global_load_dwordx4 v[132:135], v[232:233], off offset:1024
	v_add_u32_e32 v234, 0x20000, v250
	v_ashrrev_i32_e32 v235, 31, v234
	v_lshlrev_b64 v[234:235], 11, v[234:235]
	v_lshl_add_u64 v[234:235], v[86:87], 0, v[234:235]
	global_load_dwordx4 v[168:171], v[234:235], off
	global_load_dwordx4 v[128:131], v[234:235], off offset:1024
	v_readlane_b32 s98, v248, 0
	s_ashr_i32 s99, s98, 31
	s_lshl_b64 s[98:99], s[98:99], 11
	v_lshl_add_u64 v[234:235], v[86:87], 0, s[98:99]
	global_load_dwordx4 v[176:179], v[234:235], off
	global_load_dwordx4 v[140:143], v[234:235], off offset:1024
	v_readlane_b32 s98, v248, 1
	s_ashr_i32 s99, s98, 31
	s_lshl_b64 s[98:99], s[98:99], 11
	v_lshl_add_u64 v[234:235], v[86:87], 0, s[98:99]
	global_load_dwordx4 v[180:183], v[234:235], off
	global_load_dwordx4 v[148:151], v[234:235], off offset:1024
	v_readlane_b32 s98, v248, 2
	s_ashr_i32 s99, s98, 31
	s_lshl_b64 s[98:99], s[98:99], 11
	v_lshl_add_u64 v[234:235], v[86:87], 0, s[98:99]
	global_load_dwordx4 v[188:191], v[234:235], off
	global_load_dwordx4 v[156:159], v[234:235], off offset:1024
	v_readlane_b32 s98, v248, 3
	s_ashr_i32 s99, s98, 31
	s_lshl_b64 s[98:99], s[98:99], 11
	v_lshl_add_u64 v[234:235], v[86:87], 0, s[98:99]
	global_load_dwordx4 v[192:195], v[234:235], off
	global_load_dwordx4 v[160:163], v[234:235], off offset:1024
	v_readlane_b32 s98, v248, 4
	s_ashr_i32 s99, s98, 31
	s_lshl_b64 s[98:99], s[98:99], 11
	v_lshl_add_u64 v[234:235], v[86:87], 0, s[98:99]
	global_load_dwordx4 v[196:199], v[234:235], off
	global_load_dwordx4 v[164:167], v[234:235], off offset:1024
	v_readlane_b32 s98, v248, 5
	s_ashr_i32 s99, s98, 31
	s_lshl_b64 s[98:99], s[98:99], 11
	v_lshl_add_u64 v[234:235], v[86:87], 0, s[98:99]
	global_load_dwordx4 v[136:139], v[234:235], off
	global_load_dwordx4 v[120:123], v[234:235], off offset:1024
	v_readlane_b32 s98, v248, 6
	s_ashr_i32 s99, s98, 31
	s_lshl_b64 s[98:99], s[98:99], 11
	v_lshl_add_u64 v[234:235], v[86:87], 0, s[98:99]
	global_load_dwordx4 v[152:155], v[234:235], off
	global_load_dwordx4 v[124:127], v[234:235], off offset:1024
	v_readlane_b32 s98, v248, 7
	s_ashr_i32 s99, s98, 31
	s_lshl_b64 s[98:99], s[98:99], 11
	v_lshl_add_u64 v[234:235], v[86:87], 0, s[98:99]
	global_load_dwordx4 v[184:187], v[234:235], off
	global_load_dwordx4 v[144:147], v[234:235], off offset:1024
	v_add_u32_e32 v88, s9, v88
	v_min_u32_e32 v240, 0x1ffff, v88
	v_mov_b32_e32 v241, 0
	v_readlane_b32 s98, v253, 55
	v_readlane_b32 s99, v253, 56
	v_lshlrev_b64 v[240:241], 2, v[240:241]
	s_nop 1
	v_lshl_add_u64 v[242:243], s[98:99], 0, v[240:241]
	global_load_dword v244, v[242:243], off
	v_readlane_b32 s98, v253, 59
	v_readlane_b32 s99, v253, 60
	s_nop 1
	v_lshl_add_u64 v[242:243], s[98:99], 0, v[240:241]
	global_load_dword v245, v[242:243], off
	v_readlane_b32 s98, v253, 57
	v_readlane_b32 s99, v253, 58
	s_nop 1
	v_lshl_add_u64 v[242:243], s[98:99], 0, v[240:241]
	global_load_dword v246, v[242:243], off
	v_lshlrev_b32_e32 v92, 16, v52
	v_and_b32_e32 v93, 0xffff0000, v52
	v_lshlrev_b32_e32 v94, 16, v48
	v_and_b32_e32 v95, 0xffff0000, v48
	v_lshlrev_b32_e32 v52, 16, v53
	v_and_b32_e32 v53, 0xffff0000, v53
	v_lshlrev_b32_e32 v48, 16, v49
	v_and_b32_e32 v49, 0xffff0000, v49
	v_pk_fma_f32 v[48:49], v[52:53], s[8:9], v[48:49] op_sel_hi:[1,0,1]
	v_lshlrev_b32_e32 v52, 16, v57
	v_and_b32_e32 v53, 0xffff0000, v57
	v_pk_fma_f32 v[102:103], s[24:25], v[52:53], v[48:49] op_sel_hi:[0,1,1]
	v_lshlrev_b32_e32 v48, 16, v54
	v_and_b32_e32 v49, 0xffff0000, v54
	v_lshlrev_b32_e32 v52, 16, v50
	v_and_b32_e32 v53, 0xffff0000, v50
	v_pk_fma_f32 v[48:49], v[48:49], s[8:9], v[52:53] op_sel_hi:[1,0,1]
	v_lshlrev_b32_e32 v52, 16, v58
	v_and_b32_e32 v53, 0xffff0000, v58
	v_pk_fma_f32 v[104:105], s[24:25], v[52:53], v[48:49] op_sel_hi:[0,1,1]
	v_lshlrev_b32_e32 v48, 16, v55
	v_and_b32_e32 v49, 0xffff0000, v55
	v_lshlrev_b32_e32 v50, 16, v51
	v_and_b32_e32 v51, 0xffff0000, v51
	v_pk_fma_f32 v[48:49], v[48:49], s[8:9], v[50:51] op_sel_hi:[1,0,1]
	v_lshlrev_b32_e32 v50, 16, v59
	v_and_b32_e32 v51, 0xffff0000, v59
	v_pk_fma_f32 v[58:59], s[24:25], v[50:51], v[48:49] op_sel_hi:[0,1,1]
	v_lshlrev_b32_e32 v48, 16, v12
	v_and_b32_e32 v49, 0xffff0000, v12
	v_lshlrev_b32_e32 v50, 16, v8
	v_and_b32_e32 v51, 0xffff0000, v8
	v_lshlrev_b32_e32 v12, 16, v13
	v_and_b32_e32 v13, 0xffff0000, v13
	v_lshlrev_b32_e32 v8, 16, v9
	v_and_b32_e32 v9, 0xffff0000, v9
	v_pk_fma_f32 v[48:49], v[48:49], s[8:9], v[50:51] op_sel_hi:[1,0,1]
	v_lshlrev_b32_e32 v50, 16, v20
	v_and_b32_e32 v51, 0xffff0000, v20
	v_pk_fma_f32 v[8:9], v[12:13], s[8:9], v[8:9] op_sel_hi:[1,0,1]
	v_lshlrev_b32_e32 v12, 16, v21
	v_and_b32_e32 v13, 0xffff0000, v21
	v_pk_fma_f32 v[92:93], v[92:93], s[8:9], v[94:95] op_sel_hi:[1,0,1]
	v_lshlrev_b32_e32 v94, 16, v56
	v_and_b32_e32 v95, 0xffff0000, v56
	v_pk_fma_f32 v[48:49], s[24:25], v[50:51], v[48:49] op_sel_hi:[0,1,1]
	v_lshlrev_b32_e32 v54, 16, v28
	v_and_b32_e32 v55, 0xffff0000, v28
	v_lshlrev_b32_e32 v56, 16, v36
	v_and_b32_e32 v57, 0xffff0000, v36
	v_lshlrev_b32_e32 v52, 16, v40
	v_and_b32_e32 v53, 0xffff0000, v40
	v_lshlrev_b32_e32 v50, 16, v44
	v_and_b32_e32 v51, 0xffff0000, v44
	v_pk_fma_f32 v[8:9], s[24:25], v[12:13], v[8:9] op_sel_hi:[0,1,1]
	v_lshlrev_b32_e32 v12, 16, v29
	v_and_b32_e32 v13, 0xffff0000, v29
	v_lshlrev_b32_e32 v20, 16, v37
	v_and_b32_e32 v21, 0xffff0000, v37
	v_lshlrev_b32_e32 v28, 16, v41
	v_and_b32_e32 v29, 0xffff0000, v41
	v_lshlrev_b32_e32 v36, 16, v45
	v_and_b32_e32 v37, 0xffff0000, v45
	v_lshlrev_b32_e32 v40, 16, v14
	v_and_b32_e32 v41, 0xffff0000, v14
	v_lshlrev_b32_e32 v44, 16, v10
	v_and_b32_e32 v45, 0xffff0000, v10
	v_lshlrev_b32_e32 v14, 16, v15
	v_and_b32_e32 v15, 0xffff0000, v15
	v_lshlrev_b32_e32 v10, 16, v11
	v_and_b32_e32 v11, 0xffff0000, v11
	v_lshlrev_b32_e32 v106, 16, v62
	v_and_b32_e32 v107, 0xffff0000, v62
	v_lshlrev_b32_e32 v62, 16, v63
	v_and_b32_e32 v63, 0xffff0000, v63
	v_pk_fma_f32 v[40:41], v[40:41], s[8:9], v[44:45] op_sel_hi:[1,0,1]
	v_lshlrev_b32_e32 v44, 16, v22
	v_and_b32_e32 v45, 0xffff0000, v22
	v_pk_fma_f32 v[10:11], v[14:15], s[8:9], v[10:11] op_sel_hi:[1,0,1]
	v_lshlrev_b32_e32 v14, 16, v23
	v_and_b32_e32 v15, 0xffff0000, v23
	v_lshlrev_b32_e32 v108, 16, v70
	v_and_b32_e32 v109, 0xffff0000, v70
	v_lshlrev_b32_e32 v70, 16, v71
	v_and_b32_e32 v71, 0xffff0000, v71
	v_pk_fma_f32 v[40:41], s[24:25], v[44:45], v[40:41] op_sel_hi:[0,1,1]
	v_lshlrev_b32_e32 v44, 16, v30
	v_and_b32_e32 v45, 0xffff0000, v30
	v_lshlrev_b32_e32 v116, 16, v42
	v_and_b32_e32 v117, 0xffff0000, v42
	v_pk_fma_f32 v[10:11], s[24:25], v[14:15], v[10:11] op_sel_hi:[0,1,1]
	v_lshlrev_b32_e32 v14, 16, v31
	v_and_b32_e32 v15, 0xffff0000, v31
	v_lshlrev_b32_e32 v30, 16, v43
	v_and_b32_e32 v31, 0xffff0000, v43
	v_pk_fma_f32 v[42:43], s[10:11], v[62:63], v[58:59] op_sel_hi:[0,1,1]
	v_lshlrev_b32_e32 v110, 16, v74
	v_and_b32_e32 v111, 0xffff0000, v74
	v_lshlrev_b32_e32 v74, 16, v75
	v_and_b32_e32 v75, 0xffff0000, v75
	v_pk_fma_f32 v[42:43], s[12:13], v[70:71], v[42:43] op_sel_hi:[0,1,1]
	v_lshlrev_b32_e32 v112, 16, v78
	v_and_b32_e32 v113, 0xffff0000, v78
	v_lshlrev_b32_e32 v78, 16, v79
	v_and_b32_e32 v79, 0xffff0000, v79
	v_pk_fma_f32 v[42:43], s[14:15], v[74:75], v[42:43] op_sel_hi:[0,1,1]
	v_lshlrev_b32_e32 v114, 16, v38
	v_and_b32_e32 v115, 0xffff0000, v38
	v_lshlrev_b32_e32 v118, 16, v46
	v_and_b32_e32 v119, 0xffff0000, v46
	v_lshlrev_b32_e32 v22, 16, v39
	v_and_b32_e32 v23, 0xffff0000, v39
	v_lshlrev_b32_e32 v38, 16, v47
	v_and_b32_e32 v39, 0xffff0000, v47
	v_pk_fma_f32 v[42:43], s[16:17], v[78:79], v[42:43] op_sel_hi:[0,1,1]
	v_lshlrev_b32_e32 v46, 16, v19
	v_and_b32_e32 v47, 0xffff0000, v19
	v_pk_fma_f32 v[42:43], s[18:19], v[46:47], v[42:43] op_sel_hi:[0,1,1]
	v_lshlrev_b32_e32 v46, 16, v35
	v_and_b32_e32 v47, 0xffff0000, v35
	v_pk_fma_f32 v[42:43], s[20:21], v[46:47], v[42:43] op_sel_hi:[0,1,1]
	v_lshlrev_b32_e32 v46, 16, v67
	v_and_b32_e32 v47, 0xffff0000, v67
	v_pk_fma_f32 v[42:43], s[22:23], v[46:47], v[42:43] op_sel_hi:[0,1,1]
	v_pk_fma_f32 v[46:47], s[10:11], v[106:107], v[104:105] op_sel_hi:[0,1,1]
	v_pk_fma_f32 v[46:47], s[12:13], v[108:109], v[46:47] op_sel_hi:[0,1,1]
	v_pk_fma_f32 v[46:47], s[14:15], v[110:111], v[46:47] op_sel_hi:[0,1,1]
	v_pk_fma_f32 v[10:11], s[10:11], v[14:15], v[10:11] op_sel_hi:[0,1,1]
	v_pk_fma_f32 v[46:47], s[16:17], v[112:113], v[46:47] op_sel_hi:[0,1,1]
	v_lshlrev_b32_e32 v58, 16, v18
	v_and_b32_e32 v59, 0xffff0000, v18
	v_pk_fma_f32 v[10:11], s[12:13], v[22:23], v[10:11] op_sel_hi:[0,1,1]
	v_pk_fma_f32 v[18:19], s[18:19], v[58:59], v[46:47] op_sel_hi:[0,1,1]
	v_lshlrev_b32_e32 v46, 16, v34
	v_and_b32_e32 v47, 0xffff0000, v34
	v_pk_fma_f32 v[10:11], s[14:15], v[30:31], v[10:11] op_sel_hi:[0,1,1]
	v_lshlrev_b32_e32 v100, 16, v60
	v_and_b32_e32 v101, 0xffff0000, v60
	v_lshlrev_b32_e32 v60, 16, v61
	v_and_b32_e32 v61, 0xffff0000, v61
	v_pk_fma_f32 v[18:19], s[20:21], v[46:47], v[18:19] op_sel_hi:[0,1,1]
	v_lshlrev_b32_e32 v34, 16, v66
	v_and_b32_e32 v35, 0xffff0000, v66
	v_pk_fma_f32 v[10:11], s[16:17], v[38:39], v[10:11] op_sel_hi:[0,1,1]
	v_lshlrev_b32_e32 v14, 16, v3
	v_and_b32_e32 v15, 0xffff0000, v3
	v_lshlrev_b32_e32 v98, 16, v68
	v_and_b32_e32 v99, 0xffff0000, v68
	v_lshlrev_b32_e32 v68, 16, v69
	v_and_b32_e32 v69, 0xffff0000, v69
	v_pk_fma_f32 v[18:19], s[22:23], v[34:35], v[18:19] op_sel_hi:[0,1,1]
	v_pk_fma_f32 v[34:35], s[10:11], v[60:61], v[102:103] op_sel_hi:[0,1,1]
	v_pk_fma_f32 v[10:11], s[18:19], v[14:15], v[10:11] op_sel_hi:[0,1,1]
	v_lshlrev_b32_e32 v14, 16, v7
	v_and_b32_e32 v15, 0xffff0000, v7
	v_pk_fma_f32 v[96:97], s[24:25], v[94:95], v[92:93] op_sel_hi:[0,1,1]
	v_lshlrev_b32_e32 v94, 16, v72
	v_and_b32_e32 v95, 0xffff0000, v72
	v_lshlrev_b32_e32 v72, 16, v73
	v_and_b32_e32 v73, 0xffff0000, v73
	v_pk_fma_f32 v[34:35], s[12:13], v[68:69], v[34:35] op_sel_hi:[0,1,1]
	v_pk_fma_f32 v[10:11], s[20:21], v[14:15], v[10:11] op_sel_hi:[0,1,1]
	v_lshlrev_b32_e32 v14, 16, v27
	v_and_b32_e32 v15, 0xffff0000, v27
	v_lshlrev_b32_e32 v92, 16, v76
	v_and_b32_e32 v93, 0xffff0000, v76
	v_lshlrev_b32_e32 v76, 16, v77
	v_and_b32_e32 v77, 0xffff0000, v77
	v_pk_fma_f32 v[34:35], s[14:15], v[72:73], v[34:35] op_sel_hi:[0,1,1]
	v_pk_fma_f32 v[10:11], s[22:23], v[14:15], v[10:11] op_sel_hi:[0,1,1]
	v_pk_fma_f32 v[14:15], s[10:11], v[44:45], v[40:41] op_sel_hi:[0,1,1]
	v_pk_fma_f32 v[34:35], s[16:17], v[76:77], v[34:35] op_sel_hi:[0,1,1]
	v_lshlrev_b32_e32 v46, 16, v17
	v_and_b32_e32 v47, 0xffff0000, v17
	v_pk_fma_f32 v[14:15], s[12:13], v[114:115], v[14:15] op_sel_hi:[0,1,1]
	v_pk_fma_f32 v[34:35], s[18:19], v[46:47], v[34:35] op_sel_hi:[0,1,1]
	v_lshlrev_b32_e32 v46, 16, v33
	v_and_b32_e32 v47, 0xffff0000, v33
	v_pk_fma_f32 v[14:15], s[14:15], v[116:117], v[14:15] op_sel_hi:[0,1,1]
	v_pk_fma_f32 v[34:35], s[20:21], v[46:47], v[34:35] op_sel_hi:[0,1,1]
	v_lshlrev_b32_e32 v46, 16, v65
	v_and_b32_e32 v47, 0xffff0000, v65
	v_pk_fma_f32 v[14:15], s[16:17], v[118:119], v[14:15] op_sel_hi:[0,1,1]
	v_lshlrev_b32_e32 v22, 16, v2
	v_and_b32_e32 v23, 0xffff0000, v2
	v_pk_fma_f32 v[34:35], s[22:23], v[46:47], v[34:35] op_sel_hi:[0,1,1]
	v_pk_fma_f32 v[46:47], s[10:11], v[100:101], v[96:97] op_sel_hi:[0,1,1]
	v_pk_fma_f32 v[2:3], s[18:19], v[22:23], v[14:15] op_sel_hi:[0,1,1]
	v_lshlrev_b32_e32 v14, 16, v6
	v_and_b32_e32 v15, 0xffff0000, v6
	v_pk_fma_f32 v[46:47], s[12:13], v[98:99], v[46:47] op_sel_hi:[0,1,1]
	v_pk_fma_f32 v[2:3], s[20:21], v[14:15], v[2:3] op_sel_hi:[0,1,1]
	v_lshlrev_b32_e32 v6, 16, v26
	v_and_b32_e32 v7, 0xffff0000, v26
	v_pk_fma_f32 v[46:47], s[14:15], v[94:95], v[46:47] op_sel_hi:[0,1,1]
	v_pk_fma_f32 v[2:3], s[22:23], v[6:7], v[2:3] op_sel_hi:[0,1,1]
	v_pk_fma_f32 v[6:7], s[10:11], v[12:13], v[8:9] op_sel_hi:[0,1,1]
	v_pk_fma_f32 v[46:47], s[16:17], v[92:93], v[46:47] op_sel_hi:[0,1,1]
	v_lshlrev_b32_e32 v58, 16, v16
	v_and_b32_e32 v59, 0xffff0000, v16
	v_pk_fma_f32 v[6:7], s[12:13], v[20:21], v[6:7] op_sel_hi:[0,1,1]
	v_pk_fma_f32 v[16:17], s[18:19], v[58:59], v[46:47] op_sel_hi:[0,1,1]
	v_lshlrev_b32_e32 v46, 16, v32
	v_and_b32_e32 v47, 0xffff0000, v32
	v_pk_fma_f32 v[6:7], s[14:15], v[28:29], v[6:7] op_sel_hi:[0,1,1]
	v_pk_fma_f32 v[16:17], s[20:21], v[46:47], v[16:17] op_sel_hi:[0,1,1]
	v_lshlrev_b32_e32 v32, 16, v64
	v_and_b32_e32 v33, 0xffff0000, v64
	v_pk_fma_f32 v[6:7], s[16:17], v[36:37], v[6:7] op_sel_hi:[0,1,1]
	v_lshlrev_b32_e32 v8, 16, v1
	v_and_b32_e32 v9, 0xffff0000, v1
	v_pk_fma_f32 v[16:17], s[22:23], v[32:33], v[16:17] op_sel_hi:[0,1,1]
	v_pk_fma_f32 v[6:7], s[18:19], v[8:9], v[6:7] op_sel_hi:[0,1,1]
	v_lshlrev_b32_e32 v8, 16, v5
	v_and_b32_e32 v9, 0xffff0000, v5
	v_add_f32_e32 v32, 0, v16
	v_pk_fma_f32 v[6:7], s[20:21], v[8:9], v[6:7] op_sel_hi:[0,1,1]
	v_lshlrev_b32_e32 v8, 16, v25
	v_and_b32_e32 v9, 0xffff0000, v25
	v_add_f32_e32 v32, v17, v32
	v_pk_fma_f32 v[6:7], s[22:23], v[8:9], v[6:7] op_sel_hi:[0,1,1]
	v_pk_fma_f32 v[8:9], s[10:11], v[54:55], v[48:49] op_sel_hi:[0,1,1]
	v_add_f32_e32 v32, v34, v32
	v_pk_fma_f32 v[8:9], s[12:13], v[56:57], v[8:9] op_sel_hi:[0,1,1]
	v_add_f32_e32 v32, v35, v32
	v_pk_fma_f32 v[8:9], s[14:15], v[52:53], v[8:9] op_sel_hi:[0,1,1]
	v_add_f32_e32 v32, v18, v32
	v_pk_fma_f32 v[8:9], s[16:17], v[50:51], v[8:9] op_sel_hi:[0,1,1]
	v_lshlrev_b32_e32 v12, 16, v0
	v_and_b32_e32 v13, 0xffff0000, v0
	v_add_f32_e32 v32, v19, v32
	v_pk_fma_f32 v[0:1], s[18:19], v[12:13], v[8:9] op_sel_hi:[0,1,1]
	v_lshlrev_b32_e32 v8, 16, v4
	v_and_b32_e32 v9, 0xffff0000, v4
	v_add_f32_e32 v32, v42, v32
	v_pk_fma_f32 v[0:1], s[20:21], v[8:9], v[0:1] op_sel_hi:[0,1,1]
	v_lshlrev_b32_e32 v4, 16, v24
	v_and_b32_e32 v5, 0xffff0000, v24
	v_add_f32_e32 v32, v43, v32
	v_pk_fma_f32 v[0:1], s[22:23], v[4:5], v[0:1] op_sel_hi:[0,1,1]
	v_add_f32_e32 v4, v0, v32
	v_add_f32_e32 v4, v1, v4
	v_add_f32_e32 v4, v6, v4
	v_add_f32_e32 v4, v7, v4
	v_add_f32_e32 v4, v2, v4
	v_add_f32_e32 v4, v3, v4
	v_add_f32_e32 v4, v10, v4
	v_add_f32_e32 v4, v11, v4
	s_mov_b32 s10, 0x800000
	s_nop 0
	v_add_f32_dpp v4, v4, v4 quad_perm:[1,0,3,2] row_mask:0xf bank_mask:0xf bound_ctrl:1
	s_nop 1
	v_add_f32_dpp v4, v4, v4 quad_perm:[2,3,0,1] row_mask:0xf bank_mask:0xf bound_ctrl:1
	s_nop 1
	v_add_f32_dpp v4, v4, v4 row_half_mirror row_mask:0xf bank_mask:0xf bound_ctrl:1
	s_nop 1
	v_add_f32_dpp v4, v4, v4 row_mirror row_mask:0xf bank_mask:0xf bound_ctrl:1
	v_mov_b32_e32 v5, v4
	s_nop 1
	v_permlane16_swap_b32 v5, v4
	s_nop 0
	v_add_f32_e32 v4, v5, v4
	v_mov_b32_e32 v5, v4
	s_nop 1
	v_permlane32_swap_b32 v4, v5
	s_nop 0
	v_add_f32_e32 v4, v4, v5
	v_mul_f32_e32 v4, 0x3a800000, v4
	v_pk_add_f32 v[26:27], v[16:17], v[4:5] op_sel_hi:[1,0] neg_lo:[0,1] neg_hi:[0,1]
	v_pk_add_f32 v[28:29], v[34:35], v[4:5] op_sel_hi:[1,0] neg_lo:[0,1] neg_hi:[0,1]
	v_pk_mul_f32 v[8:9], v[26:27], v[26:27]
	v_pk_mul_f32 v[12:13], v[28:29], v[28:29]
	v_add_f32_e32 v8, v8, v9
	v_pk_add_f32 v[30:31], v[18:19], v[4:5] op_sel_hi:[1,0] neg_lo:[0,1] neg_hi:[0,1]
	v_add_f32_e32 v8, v12, v8
	v_pk_mul_f32 v[14:15], v[30:31], v[30:31]
	v_add_f32_e32 v8, v13, v8
	v_pk_add_f32 v[32:33], v[42:43], v[4:5] op_sel_hi:[1,0] neg_lo:[0,1] neg_hi:[0,1]
	v_add_f32_e32 v8, v14, v8
	v_pk_mul_f32 v[24:25], v[32:33], v[32:33]
	v_add_f32_e32 v8, v15, v8
	v_pk_add_f32 v[16:17], v[0:1], v[4:5] op_sel_hi:[1,0] neg_lo:[0,1] neg_hi:[0,1]
	v_add_f32_e32 v8, v24, v8
	v_pk_mul_f32 v[0:1], v[16:17], v[16:17]
	v_add_f32_e32 v8, v25, v8
	v_pk_add_f32 v[18:19], v[6:7], v[4:5] op_sel_hi:[1,0] neg_lo:[0,1] neg_hi:[0,1]
	v_add_f32_e32 v0, v0, v8
	v_pk_mul_f32 v[6:7], v[18:19], v[18:19]
	v_add_f32_e32 v0, v1, v0
	v_pk_add_f32 v[20:21], v[2:3], v[4:5] op_sel_hi:[1,0] neg_lo:[0,1] neg_hi:[0,1]
	v_add_f32_e32 v0, v6, v0
	v_pk_mul_f32 v[2:3], v[20:21], v[20:21]
	v_add_f32_e32 v0, v7, v0
	v_pk_add_f32 v[22:23], v[10:11], v[4:5] op_sel_hi:[1,0] neg_lo:[0,1] neg_hi:[0,1]
	v_add_f32_e32 v0, v2, v0
	v_pk_mul_f32 v[4:5], v[22:23], v[22:23]
	v_add_f32_e32 v0, v3, v0
	v_add_f32_e32 v0, v4, v0
	v_add_f32_e32 v0, v5, v0
	s_nop 1
	v_add_f32_dpp v0, v0, v0 quad_perm:[1,0,3,2] row_mask:0xf bank_mask:0xf bound_ctrl:1
	s_nop 1
	v_add_f32_dpp v0, v0, v0 quad_perm:[2,3,0,1] row_mask:0xf bank_mask:0xf bound_ctrl:1
	s_nop 1
	v_add_f32_dpp v0, v0, v0 row_half_mirror row_mask:0xf bank_mask:0xf bound_ctrl:1
	s_nop 1
	v_add_f32_dpp v0, v0, v0 row_mirror row_mask:0xf bank_mask:0xf bound_ctrl:1
	v_mov_b32_e32 v1, v0
	s_nop 1
	v_permlane16_swap_b32 v1, v0
	s_nop 0
	v_add_f32_e32 v0, v1, v0
	v_mov_b32_e32 v1, v0
	s_nop 1
	v_permlane32_swap_b32 v1, v0
	s_nop 0
	v_add_f32_e32 v0, v1, v0
	v_fmamk_f32 v0, v0, 0x3a800000, v81
	v_cmp_gt_f32_e32 vcc, s10, v0
	v_mul_f32_e32 v1, 0x4b800000, v0
	s_mov_b32 s10, 0xf2b00000
	v_cndmask_b32_e32 v0, v0, v1, vcc
	v_rsq_f32_e32 v0, v0
	s_nop 0
	v_mul_f32_e32 v1, 0x45800000, v0
	v_cndmask_b32_e32 v24, v0, v1, vcc
	v_pk_mul_f32 v[26:27], v[26:27], v[24:25] op_sel_hi:[1,0]
	v_pk_mul_f32 v[16:17], v[16:17], v[24:25] op_sel_hi:[1,0]
	v_pk_fma_f32 v[8:9], v[200:201], v[26:27], v[208:209]
	v_pk_mul_f32 v[12:13], v[28:29], v[24:25] op_sel_hi:[1,0]
	s_nop 0
	v_pk_fma_f32 v[10:11], v[202:203], v[12:13], v[210:211]
	v_pk_mul_f32 v[12:13], v[30:31], v[24:25] op_sel_hi:[1,0]
	s_nop 0
	v_pk_fma_f32 v[4:5], v[204:205], v[12:13], v[212:213]
	v_pk_mul_f32 v[0:1], v[32:33], v[24:25] op_sel_hi:[1,0]
	s_nop 0
	v_pk_fma_f32 v[6:7], v[0:1], v[206:207], v[214:215]
	v_cvt_pk_bf16_f32 v2, v4, v5
	v_add_co_u32_e32 v4, vcc, s10, v90
	v_cvt_pk_bf16_f32 v0, v8, v9
	v_cvt_pk_bf16_f32 v1, v10, v11
	v_cvt_pk_bf16_f32 v3, v6, v7
	v_addc_co_u32_e32 v5, vcc, -1, v91, vcc
	global_store_dwordx4 v[4:5], v[0:3], off
	s_movk_i32 s10, 0x3fff
	v_pk_fma_f32 v[4:5], v[16:17], v[216:217], v[224:225]
	v_pk_mul_f32 v[12:13], v[18:19], v[24:25] op_sel_hi:[1,0]
	s_nop 0
	v_pk_fma_f32 v[6:7], v[12:13], v[218:219], v[226:227]
	v_pk_mul_f32 v[12:13], v[20:21], v[24:25] op_sel_hi:[1,0]
	s_nop 0
	v_pk_fma_f32 v[8:9], v[12:13], v[220:221], v[228:229]
	v_pk_mul_f32 v[0:1], v[22:23], v[24:25] op_sel_hi:[1,0]
	s_nop 0
	v_pk_fma_f32 v[10:11], v[0:1], v[222:223], v[230:231]
	v_cvt_pk_bf16_f32 v0, v4, v5
	v_add_co_u32_e32 v4, vcc, 0xf2b01000, v90
	v_cvt_pk_bf16_f32 v1, v6, v7
	s_nop 0
	v_addc_co_u32_e32 v5, vcc, -1, v91, vcc
	v_cmp_lt_i32_e32 vcc, s10, v80
	v_cvt_pk_bf16_f32 v2, v8, v9
	v_cvt_pk_bf16_f32 v3, v10, v11
	v_lshl_add_u64 v[90:91], v[90:91], 0, s[4:5]
	s_or_b64 s[6:7], vcc, s[6:7]
	global_store_dwordx4 v[4:5], v[0:3], off offset:-3072
	s_andn2_b64 exec, exec, s[6:7]
	s_cbranch_execz .LBB0_1014
	s_branch .Lopt21_cb0_top
